# same as previous plus the six GEMM K-loop headers aligned to 64 bytes
# speedup vs baseline: 1.0042x; 1.0042x over previous
.LBB0_193:
	s_ashr_i32 s57, s56, 31
	s_lshl_b64 s[10:11], s[56:57], 19
	s_add_u32 s60, s77, s10
	s_addc_u32 s61, s78, s11
	s_and_b64 s[10:11], s[58:59], exec
	s_cselect_b32 s57, s61, s93
	s_cselect_b32 vcc_lo, s60, s92
	s_ashr_i32 s55, s54, 31
	s_lshl_b64 s[10:11], s[54:55], 19
	s_add_u32 s62, s79, s10
	s_addc_u32 s63, s81, s11
	s_and_b64 s[10:11], s[58:59], exec
	s_cselect_b32 s55, s63, s95
	s_cselect_b32 vcc_hi, s62, s94
	s_add_u32 s92, s92, 0x60080
	s_addc_u32 s93, s93, 0
	s_add_u32 s10, s94, 0x100
	v_mov_b32_e32 v2, 0
	s_addc_u32 s11, s95, 0
	s_mov_b32 s1, -2
	v_mov_b32_e32 v3, v2
	v_mov_b32_e32 v4, v2
	v_mov_b32_e32 v5, v2
	v_mov_b32_e32 v6, v2
	v_mov_b32_e32 v7, v2
	v_mov_b32_e32 v8, v2
	v_mov_b32_e32 v9, v2
	v_mov_b32_e32 v10, v2
	v_mov_b32_e32 v11, v2
	v_mov_b32_e32 v12, v2
	v_mov_b32_e32 v13, v2
	v_mov_b32_e32 v14, v2
	v_mov_b32_e32 v15, v2
	v_mov_b32_e32 v16, v2
	v_mov_b32_e32 v17, v2
	v_mov_b32_e32 v26, v2
	v_mov_b32_e32 v27, v2
	v_mov_b32_e32 v28, v2
	v_mov_b32_e32 v29, v2
	v_mov_b32_e32 v30, v2
	v_mov_b32_e32 v31, v2
	v_mov_b32_e32 v32, v2
	v_mov_b32_e32 v33, v2
	v_mov_b32_e32 v42, v2
	v_mov_b32_e32 v43, v2
	v_mov_b32_e32 v44, v2
	v_mov_b32_e32 v45, v2
	v_mov_b32_e32 v54, v2
	v_mov_b32_e32 v55, v2
	v_mov_b32_e32 v56, v2
	v_mov_b32_e32 v57, v2
	v_mov_b32_e32 v58, v2
	v_mov_b32_e32 v59, v2
	v_mov_b32_e32 v60, v2
	v_mov_b32_e32 v61, v2
	v_mov_b32_e32 v62, v2
	v_mov_b32_e32 v63, v2
	v_mov_b32_e32 v64, v2
	v_mov_b32_e32 v65, v2
	v_mov_b32_e32 v78, v2
	v_mov_b32_e32 v79, v2
	v_mov_b32_e32 v80, v2
	v_mov_b32_e32 v81, v2
	v_mov_b32_e32 v86, v2
	v_mov_b32_e32 v87, v2
	v_mov_b32_e32 v88, v2
	v_mov_b32_e32 v89, v2
	v_mov_b32_e32 v94, v2
	v_mov_b32_e32 v95, v2
	v_mov_b32_e32 v96, v2
	v_mov_b32_e32 v97, v2
	v_mov_b32_e32 v102, v2
	v_mov_b32_e32 v103, v2
	v_mov_b32_e32 v104, v2
	v_mov_b32_e32 v105, v2
	v_mov_b32_e32 v110, v2
	v_mov_b32_e32 v111, v2
	v_mov_b32_e32 v112, v2
	v_mov_b32_e32 v113, v2
	v_mov_b32_e32 v118, v2
	v_mov_b32_e32 v119, v2
	v_mov_b32_e32 v120, v2
	v_mov_b32_e32 v121, v2
	v_mov_b32_e32 v74, v2
	v_mov_b32_e32 v75, v2
	v_mov_b32_e32 v76, v2
	v_mov_b32_e32 v77, v2
	v_mov_b32_e32 v82, v2
	v_mov_b32_e32 v83, v2
	v_mov_b32_e32 v84, v2
	v_mov_b32_e32 v85, v2
	v_mov_b32_e32 v90, v2
	v_mov_b32_e32 v91, v2
	v_mov_b32_e32 v92, v2
	v_mov_b32_e32 v93, v2
	v_mov_b32_e32 v98, v2
	v_mov_b32_e32 v99, v2
	v_mov_b32_e32 v100, v2
	v_mov_b32_e32 v101, v2
	v_mov_b32_e32 v106, v2
	v_mov_b32_e32 v107, v2
	v_mov_b32_e32 v108, v2
	v_mov_b32_e32 v109, v2
	v_mov_b32_e32 v114, v2
	v_mov_b32_e32 v115, v2
	v_mov_b32_e32 v116, v2
	v_mov_b32_e32 v117, v2
	v_mov_b32_e32 v122, v2
	v_mov_b32_e32 v123, v2
	v_mov_b32_e32 v124, v2
	v_mov_b32_e32 v125, v2
	v_mov_b32_e32 v126, v2
	v_mov_b32_e32 v127, v2
	v_mov_b32_e32 v128, v2
	v_mov_b32_e32 v129, v2
	v_mov_b32_e32 v66, v2
	v_mov_b32_e32 v67, v2
	v_mov_b32_e32 v68, v2
	v_mov_b32_e32 v69, v2
	v_mov_b32_e32 v70, v2
	v_mov_b32_e32 v71, v2
	v_mov_b32_e32 v72, v2
	v_mov_b32_e32 v73, v2
	v_mov_b32_e32 v46, v2
	v_mov_b32_e32 v47, v2
	v_mov_b32_e32 v48, v2
	v_mov_b32_e32 v49, v2
	v_mov_b32_e32 v50, v2
	v_mov_b32_e32 v51, v2
	v_mov_b32_e32 v52, v2
	v_mov_b32_e32 v53, v2
	v_mov_b32_e32 v34, v2
	v_mov_b32_e32 v35, v2
	v_mov_b32_e32 v36, v2
	v_mov_b32_e32 v37, v2
	v_mov_b32_e32 v38, v2
	v_mov_b32_e32 v39, v2
	v_mov_b32_e32 v40, v2
	v_mov_b32_e32 v41, v2
	v_mov_b32_e32 v18, v2
	v_mov_b32_e32 v19, v2
	v_mov_b32_e32 v20, v2
	v_mov_b32_e32 v21, v2
	v_mov_b32_e32 v22, v2
	v_mov_b32_e32 v23, v2
	v_mov_b32_e32 v24, v2
	v_mov_b32_e32 v25, v2
	.p2align	6

.LBB0_976:
	s_ashr_i32 s47, s46, 31
	s_lshl_b64 s[34:35], s[46:47], 18
	s_cmp_eq_u32 s94, 0
	s_cselect_b32 s39, s3, s77
	s_cselect_b32 s38, s4, s78
	s_cselect_b32 s47, s33, s81
	s_cselect_b32 s54, s5, s79
	s_add_u32 s50, s39, s34
	s_addc_u32 s51, s38, s35
	s_and_b64 s[34:35], s[6:7], exec
	s_cselect_b32 s38, s51, s59
	s_cselect_b32 s39, s50, s58
	s_ashr_i32 s45, s44, 31
	s_lshl_b64 s[34:35], s[44:45], 18
	s_add_u32 s54, s54, s34
	s_addc_u32 s55, s47, s35
	s_and_b64 s[34:35], s[6:7], exec
	s_cselect_b32 s45, s55, s61
	s_cselect_b32 s47, s54, s60
	s_add_u32 s58, s58, 0x30080
	s_addc_u32 s59, s59, 0
	s_add_u32 s68, s60, 0x100
	s_addc_u32 s69, s61, 0
	s_mov_b32 s70, -2
	.p2align	6

.LBB0_1073:
	s_ashr_i32 s43, s42, 31
	s_lshl_b64 s[34:35], s[42:43], 19
	s_add_u32 s44, s3, s34
	s_addc_u32 s45, s4, s35
	s_and_b64 s[34:35], s[6:7], exec
	s_cselect_b32 s38, s45, s55
	s_cselect_b32 s39, s44, s54
	s_ashr_i32 s41, s40, 31
	s_lshl_b64 s[34:35], s[40:41], 19
	s_add_u32 s46, s5, s34
	s_addc_u32 s47, s33, s35
	s_and_b64 s[34:35], s[6:7], exec
	s_cselect_b32 s41, s47, s57
	s_cselect_b32 s43, s46, s56
	s_add_u32 s54, s54, 0x60080
	s_addc_u32 s55, s55, 0
	s_add_u32 s74, s56, 0x100
	v_mov_b32_e32 v2, 0
	s_addc_u32 s75, s57, 0
	s_mov_b32 s76, -2
	v_mov_b32_e32 v3, v2
	v_mov_b32_e32 v4, v2
	v_mov_b32_e32 v5, v2
	v_mov_b32_e32 v6, v2
	v_mov_b32_e32 v7, v2
	v_mov_b32_e32 v8, v2
	v_mov_b32_e32 v9, v2
	v_mov_b32_e32 v10, v2
	v_mov_b32_e32 v11, v2
	v_mov_b32_e32 v12, v2
	v_mov_b32_e32 v13, v2
	v_mov_b32_e32 v18, v2
	v_mov_b32_e32 v19, v2
	v_mov_b32_e32 v20, v2
	v_mov_b32_e32 v21, v2
	v_mov_b32_e32 v30, v2
	v_mov_b32_e32 v31, v2
	v_mov_b32_e32 v32, v2
	v_mov_b32_e32 v33, v2
	s_waitcnt vmcnt(0)
	v_mov_b32_e32 v38, v2
	v_mov_b32_e32 v39, v2
	v_mov_b32_e32 v40, v2
	v_mov_b32_e32 v41, v2
	v_mov_b32_e32 v50, v2
	v_mov_b32_e32 v51, v2
	v_mov_b32_e32 v52, v2
	v_mov_b32_e32 v53, v2
	v_mov_b32_e32 v54, v2
	v_mov_b32_e32 v55, v2
	v_mov_b32_e32 v56, v2
	v_mov_b32_e32 v57, v2
	v_mov_b32_e32 v66, v2
	v_mov_b32_e32 v67, v2
	v_mov_b32_e32 v68, v2
	v_mov_b32_e32 v69, v2
	v_mov_b32_e32 v70, v2
	v_mov_b32_e32 v71, v2
	v_mov_b32_e32 v72, v2
	v_mov_b32_e32 v73, v2
	v_mov_b32_e32 v78, v2
	v_mov_b32_e32 v79, v2
	v_mov_b32_e32 v80, v2
	v_mov_b32_e32 v81, v2
	v_mov_b32_e32 v86, v2
	v_mov_b32_e32 v87, v2
	v_mov_b32_e32 v88, v2
	v_mov_b32_e32 v89, v2
	v_mov_b32_e32 v94, v2
	v_mov_b32_e32 v95, v2
	v_mov_b32_e32 v96, v2
	v_mov_b32_e32 v97, v2
	v_mov_b32_e32 v102, v2
	v_mov_b32_e32 v103, v2
	v_mov_b32_e32 v104, v2
	v_mov_b32_e32 v105, v2
	v_mov_b32_e32 v110, v2
	v_mov_b32_e32 v111, v2
	v_mov_b32_e32 v112, v2
	v_mov_b32_e32 v113, v2
	v_mov_b32_e32 v118, v2
	v_mov_b32_e32 v119, v2
	v_mov_b32_e32 v120, v2
	v_mov_b32_e32 v121, v2
	v_mov_b32_e32 v74, v2
	v_mov_b32_e32 v75, v2
	v_mov_b32_e32 v76, v2
	v_mov_b32_e32 v77, v2
	v_mov_b32_e32 v82, v2
	v_mov_b32_e32 v83, v2
	v_mov_b32_e32 v84, v2
	v_mov_b32_e32 v85, v2
	v_mov_b32_e32 v90, v2
	v_mov_b32_e32 v91, v2
	v_mov_b32_e32 v92, v2
	v_mov_b32_e32 v93, v2
	v_mov_b32_e32 v98, v2
	v_mov_b32_e32 v99, v2
	v_mov_b32_e32 v100, v2
	v_mov_b32_e32 v101, v2
	v_mov_b32_e32 v106, v2
	v_mov_b32_e32 v107, v2
	v_mov_b32_e32 v108, v2
	v_mov_b32_e32 v109, v2
	v_mov_b32_e32 v114, v2
	v_mov_b32_e32 v115, v2
	v_mov_b32_e32 v116, v2
	v_mov_b32_e32 v117, v2
	v_mov_b32_e32 v122, v2
	v_mov_b32_e32 v123, v2
	v_mov_b32_e32 v124, v2
	v_mov_b32_e32 v125, v2
	v_mov_b32_e32 v126, v2
	v_mov_b32_e32 v127, v2
	v_mov_b32_e32 v128, v2
	v_mov_b32_e32 v129, v2
	v_mov_b32_e32 v62, v2
	v_mov_b32_e32 v63, v2
	v_mov_b32_e32 v64, v2
	v_mov_b32_e32 v65, v2
	v_mov_b32_e32 v58, v2
	v_mov_b32_e32 v59, v2
	v_mov_b32_e32 v60, v2
	v_mov_b32_e32 v61, v2
	v_mov_b32_e32 v46, v2
	v_mov_b32_e32 v47, v2
	v_mov_b32_e32 v48, v2
	v_mov_b32_e32 v49, v2
	v_mov_b32_e32 v42, v2
	v_mov_b32_e32 v43, v2
	v_mov_b32_e32 v44, v2
	v_mov_b32_e32 v45, v2
	v_mov_b32_e32 v34, v2
	v_mov_b32_e32 v35, v2
	v_mov_b32_e32 v36, v2
	v_mov_b32_e32 v37, v2
	v_mov_b32_e32 v26, v2
	v_mov_b32_e32 v27, v2
	v_mov_b32_e32 v28, v2
	v_mov_b32_e32 v29, v2
	v_mov_b32_e32 v22, v2
	v_mov_b32_e32 v23, v2
	v_mov_b32_e32 v24, v2
	v_mov_b32_e32 v25, v2
	v_mov_b32_e32 v14, v2
	v_mov_b32_e32 v15, v2
	v_mov_b32_e32 v16, v2
	v_mov_b32_e32 v17, v2
	.p2align	6

.LBB0_1223:
	s_add_u32 s2, s58, 0x100
	s_addc_u32 s49, s59, 0
	s_mov_b32 s51, -2
	s_mov_b64 s[58:59], 0
	.p2align	6

.LBB0_1256:
	s_add_u32 s45, s54, 0x100
	s_addc_u32 s47, s55, 0
	s_mov_b32 s86, -2
	s_mov_b64 s[54:55], 0
	.p2align	6

.LBB0_1307:
	s_add_u32 s4, s4, 0x60080
	s_waitcnt vmcnt(0)
	v_pk_mul_f32 v[68:69], v[16:17], s[30:31] op_sel_hi:[1,0]
	v_pk_mul_f32 v[66:67], v[14:15], s[30:31] op_sel_hi:[1,0]
	v_pk_mul_f32 v[72:73], v[12:13], s[30:31] op_sel_hi:[1,0]
	v_pk_mul_f32 v[70:71], v[10:11], s[30:31] op_sel_hi:[1,0]
	v_pk_mul_f32 v[12:13], v[8:9], s[30:31] op_sel_hi:[1,0]
	v_pk_mul_f32 v[16:17], v[4:5], s[30:31] op_sel_hi:[1,0]
	s_addc_u32 s5, s5, 0
	v_pk_mul_f32 v[10:11], v[6:7], s[30:31] op_sel_hi:[1,0]
	v_pk_mul_f32 v[14:15], v[2:3], s[30:31] op_sel_hi:[1,0]
	s_add_u32 s41, s52, 0x100
	v_mov_b64_e32 v[28:29], v[16:17]
	v_mov_b64_e32 v[32:33], v[12:13]
	v_mov_b64_e32 v[44:45], v[16:17]
	v_mov_b64_e32 v[48:49], v[12:13]
	v_mov_b64_e32 v[60:61], v[16:17]
	v_mov_b64_e32 v[64:65], v[12:13]
	v_mov_b64_e32 v[84:85], v[72:73]
	v_mov_b64_e32 v[88:89], v[68:69]
	v_mov_b64_e32 v[100:101], v[72:73]
	v_mov_b64_e32 v[104:105], v[68:69]
	v_mov_b64_e32 v[116:117], v[72:73]
	v_mov_b64_e32 v[120:121], v[68:69]
	v_mov_b64_e32 v[76:77], v[16:17]
	v_mov_b64_e32 v[80:81], v[12:13]
	v_mov_b64_e32 v[92:93], v[16:17]
	v_mov_b64_e32 v[96:97], v[12:13]
	v_mov_b64_e32 v[108:109], v[16:17]
	v_mov_b64_e32 v[112:113], v[12:13]
	v_mov_b64_e32 v[124:125], v[16:17]
	v_mov_b64_e32 v[128:129], v[12:13]
	v_mov_b64_e32 v[54:55], v[66:67]
	v_mov_b64_e32 v[50:51], v[70:71]
	v_mov_b64_e32 v[38:39], v[66:67]
	v_mov_b64_e32 v[34:35], v[70:71]
	v_mov_b64_e32 v[22:23], v[66:67]
	v_mov_b64_e32 v[18:19], v[70:71]
	v_mov_b64_e32 v[6:7], v[66:67]
	v_mov_b64_e32 v[2:3], v[70:71]
	s_addc_u32 s43, s53, 0
	s_mov_b32 s83, -2
	v_mov_b64_e32 v[26:27], v[14:15]
	v_mov_b64_e32 v[30:31], v[10:11]
	v_mov_b64_e32 v[42:43], v[14:15]
	v_mov_b64_e32 v[46:47], v[10:11]
	v_mov_b64_e32 v[58:59], v[14:15]
	v_mov_b64_e32 v[62:63], v[10:11]
	v_mov_b64_e32 v[82:83], v[70:71]
	v_mov_b64_e32 v[86:87], v[66:67]
	v_mov_b64_e32 v[98:99], v[70:71]
	v_mov_b64_e32 v[102:103], v[66:67]
	v_mov_b64_e32 v[114:115], v[70:71]
	v_mov_b64_e32 v[118:119], v[66:67]
	v_mov_b64_e32 v[74:75], v[14:15]
	v_mov_b64_e32 v[78:79], v[10:11]
	v_mov_b64_e32 v[90:91], v[14:15]
	v_mov_b64_e32 v[94:95], v[10:11]
	v_mov_b64_e32 v[106:107], v[14:15]
	v_mov_b64_e32 v[110:111], v[10:11]
	v_mov_b64_e32 v[122:123], v[14:15]
	v_mov_b64_e32 v[126:127], v[10:11]
	v_mov_b64_e32 v[56:57], v[68:69]
	v_mov_b64_e32 v[52:53], v[72:73]
	v_mov_b64_e32 v[40:41], v[68:69]
	v_mov_b64_e32 v[36:37], v[72:73]
	v_mov_b64_e32 v[24:25], v[68:69]
	v_mov_b64_e32 v[20:21], v[72:73]
	v_mov_b64_e32 v[8:9], v[68:69]
	v_mov_b64_e32 v[4:5], v[72:73]
	.p2align	6
